# speedup vs baseline: 1.0219x; 1.0138x over previous
.LBB2_12:
	s_or_b64 exec, exec, s[12:13]
	v_lshlrev_b32_e32 v106, 9, v119
	v_ffbl_b32_e32 v107, v107
	v_ffbl_b32_e32 v108, v108
	v_lshlrev_b32_e32 v116, 25, v119
	v_lshl_or_b32 v107, v107, 4, v106
	v_mov_b32_e32 v109, 0x2000
	v_lshl_or_b32 v108, v108, 20, v116
	v_bfrev_b32_e32 v116, 4
	v_ffbl_b32_e32 v0, v0
	v_cndmask_b32_e64 v107, v107, v109, s[8:9]
	v_cndmask_b32_e64 v108, v108, v116, s[4:5]
	v_lshl_or_b32 v0, v0, 4, v106
	v_cndmask_b32_e32 v0, v0, v109, vcc
	v_or_b32_e32 v106, v108, v107
	v_mov_b32_e32 v108, 0x800000
	v_lshlrev_b32_e32 v107, 16, v117
	v_cndmask_b32_e64 v108, 0, v108, s[6:7]
	s_waitcnt lgkmcnt(2)
	v_lshl_or_b32 v0, v118, 24, v0
	v_or3_b32 v0, v0, v108, v107
	ds_write2_b32 v105, v106, v0 offset0:1 offset1:3
	v_cmp_ne_u32_e32 vcc, 0, v140
	v_cmp_ne_u32_e64 s[22:23], 0, v141
	v_lshlrev_b32_e32 v150, 5, v113
	v_lshl_add_u32 v155, v113, 2, v115
	v_lshlrev_b32_e32 v155, 2, v155
	v_add_u32_e32 v155, 0x11840, v155
	v_lshrrev_b64 v[146:147], v150, vcc
	v_lshrrev_b64 v[156:157], v150, s[22:23]
	v_mov_b32_e32 v151, 0x400
	v_cmp_ne_u32_e32 vcc, 0, v146
	v_cmp_ne_u32_e64 s[22:23], 0, v156
	s_nop 1
	v_cndmask_b32_e32 v146, 0, v151, vcc
	v_cndmask_b32_e64 v156, 0, v151, s[22:23]
	v_cmp_eq_u32_e32 vcc, 0, v111
	s_and_saveexec_b64 s[22:23], vcc
	ds_or_b32 v155, v146
	ds_or_b32 v155, v156 offset:32
	s_or_b64 exec, exec, s[22:23]
	s_movk_i32 s2, 0x2010
	v_mul_u32_u24_e32 v105, 0x2010, v115
	v_cmp_eq_u32_e32 vcc, 0, v114
	s_waitcnt vmcnt(22)
	ds_write_b128 v104, v[38:41] offset:32832
	s_waitcnt vmcnt(21)
	ds_write_b128 v104, v[42:45] offset:36928
	s_waitcnt vmcnt(20)
	ds_write_b128 v104, v[46:49] offset:41024
	s_waitcnt vmcnt(19)
	ds_write_b128 v104, v[50:53] offset:45120
	s_waitcnt vmcnt(18)
	ds_write_b128 v104, v[54:57] offset:49216
	s_waitcnt vmcnt(17)
	ds_write_b128 v104, v[66:69] offset:53312
	s_and_saveexec_b64 s[0:1], vcc
	v_mov_b32_e32 v38, 0
	v_mov_b32_e32 v39, v38
	v_mov_b32_e32 v40, v38
	v_mov_b32_e32 v41, v38
	ds_write_b128 v105, v[38:41] offset:8192
	s_or_b64 exec, exec, s[0:1]
	v_lshlrev_b32_e32 v40, 3, v113
	v_lshlrev_b32_e32 v67, 4, v110
	v_or_b32_e32 v38, 0x1e0, v111
	v_or_b32_e32 v0, 0x8040, v40
	v_mad_u32_u24 v66, v1, s2, v67
	v_mad_u32_u24 v38, v38, 48, v0
	s_waitcnt vmcnt(16)
	ds_write_b128 v66, v[58:61]
	s_waitcnt vmcnt(15)
	ds_write_b128 v66, v[62:65] offset:1024
	s_waitcnt vmcnt(14)
	ds_write_b128 v66, v[70:73] offset:2048
	s_waitcnt vmcnt(13)
	ds_write_b128 v66, v[74:77] offset:3072
	s_waitcnt vmcnt(12)
	ds_write_b128 v66, v[78:81] offset:4096
	s_waitcnt vmcnt(11)
	ds_write_b128 v66, v[82:85] offset:5120
	s_waitcnt vmcnt(10)
	ds_write_b128 v66, v[86:89] offset:6144
	s_waitcnt vmcnt(9)
	ds_write_b128 v66, v[90:93] offset:7168
	v_lshl_add_u32 v116, v113, 3, v105
	v_or_b32_e32 v106, 0x1e0, v111
	v_lshlrev_b32_e32 v138, 4, v106
	v_lshlrev_b32_e32 v139, 3, v106
	v_add_u32_e32 v139, 0x118c0, v139
	v_mul_u32_u24_e32 v156, 48, v106
	v_add_u32_e32 v156, v0, v156
	v_mov_b32_e32 v157, 0x1187c
	v_add_u32_e32 v137, v116, v138
	v_add_u32_e32 v138, 0x200, v138
	v_lshlrev_b32_e32 v160, 4, v111
	v_lshlrev_b32_e32 v161, 3, v111
	v_add_u32_e32 v161, 0x118c0, v161
	v_mul_u32_u24_e32 v162, 48, v111
	v_add_u32_e32 v162, v0, v162
	v_mov_b32_e32 v163, 0x11840
	v_mul_hi_u32_u24_e32 v159, 0x410, v111
	v_mul_u32_u24_e32 v158, 0x410, v111
	v_mov_b32_e32 v107, 0x82000
	v_mad_u64_u32 v[158:159], s[0:1], s20, v107, v[158:159]
	v_lshlrev_b32_e32 v107, 3, v113
	v_or_b32_e32 v158, v158, v107
	v_lshl_add_u64 v[158:159], s[14:15], 0, v[158:159]
	s_mov_b64 s[0:1], 0x79e30
	s_mov_b32 s2, 0xffff7e00
	s_mov_b32 s3, -1
	v_lshl_add_u64 v[158:159], v[158:159], 0, s[0:1]
	v_lshl_add_u32 v107, v114, 2, v163
	v_add_u32_e32 v107, -8, v107
	s_waitcnt lgkmcnt(0)
	s_barrier
	ds_read_b128 v[38:41], v138 offset:56896
	ds_read_b64 v[42:43], v139
	ds_read2_b64 v[56:59], v156 offset1:2
	ds_read_b32 v60, v107
	v_add_u32_e32 v156, 0xfffffa00, v156
	ds_read2_b64 v[52:55], v156 offset1:2
	v_add_u32_e32 v106, -2, v114
	v_cmp_gt_u32_e32 vcc, 16, v106
	s_waitcnt lgkmcnt(0)
	v_cndmask_b32_e32 v60, 0, v60, vcc
	s_nop 1
	v_readlane_b32 s4, v60, 17
	v_readlane_b32 s21, v60, 16
	v_add_u32_sdwa v92, v105, v56 dst_sel:DWORD dst_unused:UNUSED_PAD src0_sel:DWORD src1_sel:WORD_0
	v_add_u32_sdwa v93, v105, v56 dst_sel:DWORD dst_unused:UNUSED_PAD src0_sel:DWORD src1_sel:WORD_1
	v_add_u32_sdwa v106, v105, v57 dst_sel:DWORD dst_unused:UNUSED_PAD src0_sel:DWORD src1_sel:WORD_0
	v_add_u32_sdwa v107, v105, v57 dst_sel:DWORD dst_unused:UNUSED_PAD src0_sel:DWORD src1_sel:WORD_1
	v_add_u32_sdwa v108, v105, v58 dst_sel:DWORD dst_unused:UNUSED_PAD src0_sel:DWORD src1_sel:WORD_0
	v_add_u32_sdwa v109, v105, v58 dst_sel:DWORD dst_unused:UNUSED_PAD src0_sel:DWORD src1_sel:WORD_1
	v_add_u32_sdwa v88, v105, v59 dst_sel:DWORD dst_unused:UNUSED_PAD src0_sel:DWORD src1_sel:WORD_0
	v_add_u32_sdwa v89, v105, v59 dst_sel:DWORD dst_unused:UNUSED_PAD src0_sel:DWORD src1_sel:WORD_1
	ds_read_b128 v[120:123], v92
	ds_read_b128 v[124:127], v93
	ds_read_b128 v[128:131], v106
	ds_read_b128 v[132:135], v107
	ds_read_b128 v[140:143], v108
	ds_read_b128 v[144:147], v109
	ds_read_b128 v[148:151], v88
	ds_read_b128 v[152:155], v89
	v_add_u32_sdwa v88, v116, v42 dst_sel:DWORD dst_unused:UNUSED_PAD src0_sel:DWORD src1_sel:WORD_0
	v_add_u32_sdwa v89, v116, v42 dst_sel:DWORD dst_unused:UNUSED_PAD src0_sel:DWORD src1_sel:WORD_1
	v_add_u32_sdwa v90, v116, v43 dst_sel:DWORD dst_unused:UNUSED_PAD src0_sel:DWORD src1_sel:WORD_0
	v_add_u32_sdwa v91, v116, v43 dst_sel:DWORD dst_unused:UNUSED_PAD src0_sel:DWORD src1_sel:WORD_1
	v_bfe_u32 v117, v41, 16, 7
	v_add_u32_sdwa v118, v116, v39 dst_sel:DWORD dst_unused:UNUSED_PAD src0_sel:DWORD src1_sel:WORD_0
	v_add_u32_sdwa v119, v116, v39 dst_sel:DWORD dst_unused:UNUSED_PAD src0_sel:DWORD src1_sel:WORD_1
	v_add_u32_sdwa v136, v116, v41 dst_sel:DWORD dst_unused:UNUSED_PAD src0_sel:DWORD src1_sel:WORD_0
	s_and_b32 s9, s4, 0xff
	s_waitcnt lgkmcnt(0)
	v_pk_add_f32 v[120:121], v[120:121], v[124:125]
	v_pk_add_f32 v[122:123], v[122:123], v[126:127]
	v_pk_add_f32 v[128:129], v[128:129], v[132:133]
	v_pk_add_f32 v[130:131], v[130:131], v[134:135]
	v_pk_add_f32 v[140:141], v[140:141], v[144:145]
	v_pk_add_f32 v[142:143], v[142:143], v[146:147]
	v_pk_add_f32 v[148:149], v[148:149], v[152:153]
	v_pk_add_f32 v[150:151], v[150:151], v[154:155]
	s_bitcmp1_b32 s4, 8
	s_cbranch_scc1 .Lfarslow_pre
.Lfarslow_ret_pre:
	v_pk_add_f32 v[120:121], v[120:121], v[128:129]
	v_pk_add_f32 v[122:123], v[122:123], v[130:131]
	v_pk_add_f32 v[140:141], v[140:141], v[148:149]
	v_pk_add_f32 v[142:143], v[142:143], v[150:151]
	v_pk_add_f32 v[120:121], v[120:121], v[140:141]
	v_pk_add_f32 v[122:123], v[122:123], v[142:143]
	s_nop 1
	v_permlane32_swap_b32_e32 v120, v122
	v_permlane32_swap_b32_e32 v121, v123
	v_pk_add_f32 v[44:45], v[120:121], v[122:123]
	v_add_u32_e32 v138, 0xfffffe00, v138
	v_add_u32_e32 v139, 0xffffff00, v139
	v_add_u32_e32 v156, 0xfffffa00, v156
	v_lshl_add_u64 v[158:159], v[158:159], 0, s[2:3]
	s_mov_b32 s5, 15
	s_mov_b32 s5, 15
.Lit_A:
	ds_read_b64 v[68:69], v88
	ds_read_b64 v[70:71], v89
	ds_read_b64 v[72:73], v90
	ds_read_b64 v[74:75], v91
	v_add_u32_sdwa v92, v105, v52 dst_sel:DWORD dst_unused:UNUSED_PAD src0_sel:DWORD src1_sel:WORD_0
	v_add_u32_sdwa v93, v105, v52 dst_sel:DWORD dst_unused:UNUSED_PAD src0_sel:DWORD src1_sel:WORD_1
	v_add_u32_sdwa v106, v105, v53 dst_sel:DWORD dst_unused:UNUSED_PAD src0_sel:DWORD src1_sel:WORD_0
	v_add_u32_sdwa v107, v105, v53 dst_sel:DWORD dst_unused:UNUSED_PAD src0_sel:DWORD src1_sel:WORD_1
	v_add_u32_sdwa v108, v105, v54 dst_sel:DWORD dst_unused:UNUSED_PAD src0_sel:DWORD src1_sel:WORD_0
	v_add_u32_sdwa v109, v105, v54 dst_sel:DWORD dst_unused:UNUSED_PAD src0_sel:DWORD src1_sel:WORD_1
	v_add_u32_sdwa v88, v105, v55 dst_sel:DWORD dst_unused:UNUSED_PAD src0_sel:DWORD src1_sel:WORD_0
	v_add_u32_sdwa v89, v105, v55 dst_sel:DWORD dst_unused:UNUSED_PAD src0_sel:DWORD src1_sel:WORD_1
	ds_read_b128 v[120:123], v92
	ds_read_b128 v[124:127], v93
	ds_read_b128 v[128:131], v106
	ds_read_b128 v[132:135], v107
	ds_read_b128 v[140:143], v108
	ds_read_b128 v[144:147], v109
	ds_read_b128 v[148:151], v88
	ds_read_b128 v[152:155], v89
	s_waitcnt lgkmcnt(11)
	v_pk_add_f32 v[76:77], v[44:45], v[68:69]
	s_waitcnt lgkmcnt(9)
	v_pk_add_f32 v[78:79], v[70:71], v[72:73]
	s_waitcnt lgkmcnt(8)
	v_pk_add_f32 v[76:77], v[76:77], v[74:75]
	ds_read_b128 v[46:49], v138 offset:56896
	v_pk_add_f32 v[76:77], v[76:77], v[78:79]
	ds_read_b64 v[50:51], v139
	s_bitcmp1_b32 s4, 10
	s_cbranch_scc1 .Lnearslow_A
.Lnearslow_ret_A:
	v_pk_mul_f32 v[78:79], v[40:41], v[76:77] op_sel_hi:[0,1]
	v_cmp_eq_u32_e64 s[6:7], 1, v117
	ds_write_b64 v137, v[78:79]
	ds_read2_b64 v[56:59], v156 offset1:2
	ds_read_b64 v[82:83], v118
	ds_read_b64 v[84:85], v119
	ds_read_b64 v[86:87], v136
	s_waitcnt lgkmcnt(6)
	v_pk_add_f32 v[120:121], v[120:121], v[124:125]
	v_pk_add_f32 v[122:123], v[122:123], v[126:127]
	v_pk_add_f32 v[128:129], v[128:129], v[132:133]
	v_pk_add_f32 v[130:131], v[130:131], v[134:135]
	v_pk_add_f32 v[140:141], v[140:141], v[144:145]
	v_pk_add_f32 v[142:143], v[142:143], v[146:147]
	v_pk_add_f32 v[148:149], v[148:149], v[152:153]
	v_pk_add_f32 v[150:151], v[150:151], v[154:155]
	s_bitcmp1_b32 s21, 8
	s_cbranch_scc1 .Lfarslow_A
.Lfarslow_ret_A:
	v_pk_add_f32 v[120:121], v[120:121], v[128:129]
	v_pk_add_f32 v[122:123], v[122:123], v[130:131]
	v_pk_add_f32 v[140:141], v[140:141], v[148:149]
	v_pk_add_f32 v[142:143], v[142:143], v[150:151]
	v_pk_add_f32 v[120:121], v[120:121], v[140:141]
	v_pk_add_f32 v[122:123], v[122:123], v[142:143]
	v_add_u32_e32 v138, 0xfffffe00, v138
	v_add_u32_e32 v139, 0xffffff00, v139
	v_permlane32_swap_b32_e32 v120, v122
	v_permlane32_swap_b32_e32 v121, v123
	v_pk_add_f32 v[62:63], v[120:121], v[122:123]
	s_bitcmp1_b32 s4, 9
	s_cbranch_scc1 .Lslowlev_A
	s_mov_b64 exec, s[6:7]
	s_waitcnt lgkmcnt(2)
	v_pk_fma_f32 v[80:81], v[40:41], v[82:83], v[78:79] op_sel_hi:[0,1,1]
	s_waitcnt lgkmcnt(1)
	v_pk_fma_f32 v[80:81], v[40:41], v[84:85], v[80:81] op_sel_hi:[0,1,1]
	s_waitcnt lgkmcnt(0)
	v_pk_fma_f32 v[80:81], v[40:41], v[86:87], v[80:81] op_sel_hi:[0,1,1]
	ds_write_b64 v137, v[80:81]
	s_mov_b64 exec, -1
	s_cmp_lt_u32 s9, 2
	s_cbranch_scc1 .Lnp_A
	v_cmp_eq_u32_e64 s[6:7], 2, v117
	s_nop 0
	s_mov_b64 exec, s[6:7]
	ds_read_b64 v[82:83], v118
	ds_read_b64 v[84:85], v119
	ds_read_b64 v[86:87], v136
	s_mov_b64 exec, -1
	v_add_u32_sdwa v88, v116, v50 dst_sel:DWORD dst_unused:UNUSED_PAD src0_sel:DWORD src1_sel:WORD_0
	v_add_u32_sdwa v89, v116, v50 dst_sel:DWORD dst_unused:UNUSED_PAD src0_sel:DWORD src1_sel:WORD_1
	v_add_u32_sdwa v90, v116, v51 dst_sel:DWORD dst_unused:UNUSED_PAD src0_sel:DWORD src1_sel:WORD_0
	v_add_u32_sdwa v91, v116, v51 dst_sel:DWORD dst_unused:UNUSED_PAD src0_sel:DWORD src1_sel:WORD_1
	v_bfe_u32 v168, v49, 16, 7
	v_add_u32_sdwa v169, v116, v47 dst_sel:DWORD dst_unused:UNUSED_PAD src0_sel:DWORD src1_sel:WORD_0
	v_add_u32_sdwa v170, v116, v47 dst_sel:DWORD dst_unused:UNUSED_PAD src0_sel:DWORD src1_sel:WORD_1
	v_add_u32_sdwa v171, v116, v49 dst_sel:DWORD dst_unused:UNUSED_PAD src0_sel:DWORD src1_sel:WORD_0
	v_add_u32_e32 v156, 0xfffffa00, v156
	v_add_u32_e32 v172, 0xfffffe00, v137
	v_readlane_b32 s4, v60, s5
	v_max_i32_e32 v156, v156, v162
	v_lshl_add_u64 v[158:159], v[158:159], 0, s[2:3]
	s_and_b32 s23, s21, 0xff
	s_mov_b64 exec, s[6:7]
	s_waitcnt lgkmcnt(2)
	v_pk_fma_f32 v[80:81], v[40:41], v[82:83], v[78:79] op_sel_hi:[0,1,1]
	s_waitcnt lgkmcnt(1)
	v_pk_fma_f32 v[80:81], v[40:41], v[84:85], v[80:81] op_sel_hi:[0,1,1]
	s_waitcnt lgkmcnt(0)
	v_pk_fma_f32 v[80:81], v[40:41], v[86:87], v[80:81] op_sel_hi:[0,1,1]
	ds_write_b64 v137, v[80:81]
	s_mov_b64 exec, -1
	s_cmp_lt_u32 s9, 3
	s_cbranch_scc1 .Lbot_A
	s_mov_b32 s8, 3

.Lbot_A:
	s_sub_u32 s5, s5, 1
.Lit_B:
	ds_read_b64 v[68:69], v88
	ds_read_b64 v[70:71], v89
	ds_read_b64 v[72:73], v90
	ds_read_b64 v[74:75], v91
	v_add_u32_sdwa v92, v105, v56 dst_sel:DWORD dst_unused:UNUSED_PAD src0_sel:DWORD src1_sel:WORD_0
	v_add_u32_sdwa v93, v105, v56 dst_sel:DWORD dst_unused:UNUSED_PAD src0_sel:DWORD src1_sel:WORD_1
	v_add_u32_sdwa v106, v105, v57 dst_sel:DWORD dst_unused:UNUSED_PAD src0_sel:DWORD src1_sel:WORD_0
	v_add_u32_sdwa v107, v105, v57 dst_sel:DWORD dst_unused:UNUSED_PAD src0_sel:DWORD src1_sel:WORD_1
	v_add_u32_sdwa v108, v105, v58 dst_sel:DWORD dst_unused:UNUSED_PAD src0_sel:DWORD src1_sel:WORD_0
	v_add_u32_sdwa v109, v105, v58 dst_sel:DWORD dst_unused:UNUSED_PAD src0_sel:DWORD src1_sel:WORD_1
	v_add_u32_sdwa v88, v105, v59 dst_sel:DWORD dst_unused:UNUSED_PAD src0_sel:DWORD src1_sel:WORD_0
	v_add_u32_sdwa v89, v105, v59 dst_sel:DWORD dst_unused:UNUSED_PAD src0_sel:DWORD src1_sel:WORD_1
	ds_read_b128 v[120:123], v92
	ds_read_b128 v[124:127], v93
	ds_read_b128 v[128:131], v106
	ds_read_b128 v[132:135], v107
	ds_read_b128 v[140:143], v108
	ds_read_b128 v[144:147], v109
	ds_read_b128 v[148:151], v88
	ds_read_b128 v[152:155], v89
	s_waitcnt lgkmcnt(11)
	v_pk_add_f32 v[76:77], v[62:63], v[68:69]
	s_waitcnt lgkmcnt(9)
	v_pk_add_f32 v[78:79], v[70:71], v[72:73]
	s_waitcnt lgkmcnt(8)
	v_pk_add_f32 v[76:77], v[76:77], v[74:75]
	ds_read_b128 v[38:41], v138 offset:56896
	v_pk_add_f32 v[76:77], v[76:77], v[78:79]
	ds_read_b64 v[42:43], v139
	s_bitcmp1_b32 s21, 10
	s_cbranch_scc1 .Lnearslow_B
.Lnearslow_ret_B:
	v_pk_mul_f32 v[78:79], v[48:49], v[76:77] op_sel_hi:[0,1]
	v_cmp_eq_u32_e64 s[6:7], 1, v168
	ds_write_b64 v172, v[78:79]
	ds_read2_b64 v[52:55], v156 offset1:2
	ds_read_b64 v[82:83], v169
	ds_read_b64 v[84:85], v170
	ds_read_b64 v[86:87], v171
	s_waitcnt lgkmcnt(6)
	v_pk_add_f32 v[120:121], v[120:121], v[124:125]
	v_pk_add_f32 v[122:123], v[122:123], v[126:127]
	v_pk_add_f32 v[128:129], v[128:129], v[132:133]
	v_pk_add_f32 v[130:131], v[130:131], v[134:135]
	v_pk_add_f32 v[140:141], v[140:141], v[144:145]
	v_pk_add_f32 v[142:143], v[142:143], v[146:147]
	v_pk_add_f32 v[148:149], v[148:149], v[152:153]
	v_pk_add_f32 v[150:151], v[150:151], v[154:155]
	s_bitcmp1_b32 s4, 8
	s_cbranch_scc1 .Lfarslow_B
.Lfarslow_ret_B:
	v_pk_add_f32 v[120:121], v[120:121], v[128:129]
	v_pk_add_f32 v[122:123], v[122:123], v[130:131]
	v_pk_add_f32 v[140:141], v[140:141], v[148:149]
	v_pk_add_f32 v[142:143], v[142:143], v[150:151]
	v_pk_add_f32 v[120:121], v[120:121], v[140:141]
	v_pk_add_f32 v[122:123], v[122:123], v[142:143]
	v_add_u32_e32 v138, 0xfffffe00, v138
	v_add_u32_e32 v139, 0xffffff00, v139
	v_permlane32_swap_b32_e32 v120, v122
	v_permlane32_swap_b32_e32 v121, v123
	v_pk_add_f32 v[44:45], v[120:121], v[122:123]
	s_bitcmp1_b32 s21, 9
	s_cbranch_scc1 .Lslowlev_B
	s_mov_b64 exec, s[6:7]
	s_waitcnt lgkmcnt(2)
	v_pk_fma_f32 v[80:81], v[48:49], v[82:83], v[78:79] op_sel_hi:[0,1,1]
	s_waitcnt lgkmcnt(1)
	v_pk_fma_f32 v[80:81], v[48:49], v[84:85], v[80:81] op_sel_hi:[0,1,1]
	s_waitcnt lgkmcnt(0)
	v_pk_fma_f32 v[80:81], v[48:49], v[86:87], v[80:81] op_sel_hi:[0,1,1]
	ds_write_b64 v172, v[80:81]
	s_mov_b64 exec, -1
	s_cmp_lt_u32 s23, 2
	s_cbranch_scc1 .Lnp_B
	v_cmp_eq_u32_e64 s[6:7], 2, v168
	s_nop 0
	s_mov_b64 exec, s[6:7]
	ds_read_b64 v[82:83], v169
	ds_read_b64 v[84:85], v170
	ds_read_b64 v[86:87], v171
	s_mov_b64 exec, -1
	v_add_u32_sdwa v88, v116, v42 dst_sel:DWORD dst_unused:UNUSED_PAD src0_sel:DWORD src1_sel:WORD_0
	v_add_u32_sdwa v89, v116, v42 dst_sel:DWORD dst_unused:UNUSED_PAD src0_sel:DWORD src1_sel:WORD_1
	v_add_u32_sdwa v90, v116, v43 dst_sel:DWORD dst_unused:UNUSED_PAD src0_sel:DWORD src1_sel:WORD_0
	v_add_u32_sdwa v91, v116, v43 dst_sel:DWORD dst_unused:UNUSED_PAD src0_sel:DWORD src1_sel:WORD_1
	v_bfe_u32 v117, v41, 16, 7
	v_add_u32_sdwa v118, v116, v39 dst_sel:DWORD dst_unused:UNUSED_PAD src0_sel:DWORD src1_sel:WORD_0
	v_add_u32_sdwa v119, v116, v39 dst_sel:DWORD dst_unused:UNUSED_PAD src0_sel:DWORD src1_sel:WORD_1
	v_add_u32_sdwa v136, v116, v41 dst_sel:DWORD dst_unused:UNUSED_PAD src0_sel:DWORD src1_sel:WORD_0
	v_add_u32_e32 v156, 0xfffffa00, v156
	v_add_u32_e32 v137, 0xfffffe00, v172
	v_readlane_b32 s21, v60, s5
	v_max_i32_e32 v156, v156, v162
	v_lshl_add_u64 v[158:159], v[158:159], 0, s[2:3]
	s_and_b32 s9, s4, 0xff
	s_mov_b64 exec, s[6:7]
	s_waitcnt lgkmcnt(2)
	v_pk_fma_f32 v[80:81], v[48:49], v[82:83], v[78:79] op_sel_hi:[0,1,1]
	s_waitcnt lgkmcnt(1)
	v_pk_fma_f32 v[80:81], v[48:49], v[84:85], v[80:81] op_sel_hi:[0,1,1]
	s_waitcnt lgkmcnt(0)
	v_pk_fma_f32 v[80:81], v[48:49], v[86:87], v[80:81] op_sel_hi:[0,1,1]
	ds_write_b64 v172, v[80:81]
	s_mov_b64 exec, -1
	s_cmp_lt_u32 s23, 3
	s_cbranch_scc1 .Lbot_B
	s_mov_b32 s8, 3

.Lbot_B:
	s_cmp_eq_u32 s5, 0
	s_cbranch_scc1 .Lchain_done
	s_sub_u32 s5, s5, 1
	s_branch .Lit_A
.Lnp_A:
	s_waitcnt lgkmcnt(0)
	v_add_u32_sdwa v88, v116, v50 dst_sel:DWORD dst_unused:UNUSED_PAD src0_sel:DWORD src1_sel:WORD_0
	v_add_u32_sdwa v89, v116, v50 dst_sel:DWORD dst_unused:UNUSED_PAD src0_sel:DWORD src1_sel:WORD_1
	v_add_u32_sdwa v90, v116, v51 dst_sel:DWORD dst_unused:UNUSED_PAD src0_sel:DWORD src1_sel:WORD_0
	v_add_u32_sdwa v91, v116, v51 dst_sel:DWORD dst_unused:UNUSED_PAD src0_sel:DWORD src1_sel:WORD_1
	v_bfe_u32 v168, v49, 16, 7
	v_add_u32_sdwa v169, v116, v47 dst_sel:DWORD dst_unused:UNUSED_PAD src0_sel:DWORD src1_sel:WORD_0
	v_add_u32_sdwa v170, v116, v47 dst_sel:DWORD dst_unused:UNUSED_PAD src0_sel:DWORD src1_sel:WORD_1
	v_add_u32_sdwa v171, v116, v49 dst_sel:DWORD dst_unused:UNUSED_PAD src0_sel:DWORD src1_sel:WORD_0
	v_add_u32_e32 v156, 0xfffffa00, v156
	v_add_u32_e32 v172, 0xfffffe00, v137
	v_readlane_b32 s4, v60, s5
	v_max_i32_e32 v156, v156, v162
	v_lshl_add_u64 v[158:159], v[158:159], 0, s[2:3]
	s_and_b32 s23, s21, 0xff
	s_branch .Lbot_A
.Lnp_B:
	s_waitcnt lgkmcnt(0)
	v_add_u32_sdwa v88, v116, v42 dst_sel:DWORD dst_unused:UNUSED_PAD src0_sel:DWORD src1_sel:WORD_0
	v_add_u32_sdwa v89, v116, v42 dst_sel:DWORD dst_unused:UNUSED_PAD src0_sel:DWORD src1_sel:WORD_1
	v_add_u32_sdwa v90, v116, v43 dst_sel:DWORD dst_unused:UNUSED_PAD src0_sel:DWORD src1_sel:WORD_0
	v_add_u32_sdwa v91, v116, v43 dst_sel:DWORD dst_unused:UNUSED_PAD src0_sel:DWORD src1_sel:WORD_1
	v_bfe_u32 v117, v41, 16, 7
	v_add_u32_sdwa v118, v116, v39 dst_sel:DWORD dst_unused:UNUSED_PAD src0_sel:DWORD src1_sel:WORD_0
	v_add_u32_sdwa v119, v116, v39 dst_sel:DWORD dst_unused:UNUSED_PAD src0_sel:DWORD src1_sel:WORD_1
	v_add_u32_sdwa v136, v116, v41 dst_sel:DWORD dst_unused:UNUSED_PAD src0_sel:DWORD src1_sel:WORD_0
	v_add_u32_e32 v156, 0xfffffa00, v156
	v_add_u32_e32 v137, 0xfffffe00, v172
	v_readlane_b32 s21, v60, s5
	v_max_i32_e32 v156, v156, v162
	v_lshl_add_u64 v[158:159], v[158:159], 0, s[2:3]
	s_and_b32 s9, s4, 0xff
	s_branch .Lbot_B
